# all five residual epilogues pipelined (conv_out f32-base variant added) + conversion loops wait for outstanding stores before each item's loads
# speedup vs baseline: 1.0088x; 1.0088x over previous
.LBB0_761:
	v_readlane_b32 s56, v254, 51
	v_readlane_b32 s57, v254, 52
	v_readlane_b32 s70, v254, 10
	v_readlane_b32 s71, v254, 11
	v_readlane_b32 s72, v254, 12
	v_readlane_b32 s73, v254, 13
	v_readlane_b32 s74, v254, 14
	v_readlane_b32 s75, v254, 15
	v_readlane_b32 s76, v254, 16
	v_readlane_b32 s77, v254, 17
	v_readlane_b32 s78, v254, 18
	v_readlane_b32 s79, v254, 19
	v_readlane_b32 s80, v254, 20
	v_readlane_b32 s81, v254, 21
	v_readlane_b32 s82, v254, 22
	v_readlane_b32 s83, v254, 23
	v_readlane_b32 s58, v254, 53
	v_readlane_b32 s59, v254, 54
	s_ashr_i32 s13, s20, 3
	s_mul_hi_i32 s15, s13, 0xc000
	s_mul_i32 s13, s13, 0xc000
	v_lshl_or_b32 v212, s21, 8, v221
	s_add_u32 s22, s43, s13
	s_addc_u32 s23, s44, s15
	v_lshlrev_b32_e32 v213, 2, v212
	v_lshl_add_u32 v246, s20, 8, v1
	v_readlane_b32 s68, v254, 8
	v_readlane_b32 s69, v254, 9
	global_load_dwordx4 v[74:77], v213, s[22:23] offset:16
	global_load_dwordx4 v[78:81], v213, s[22:23]
	global_load_dwordx4 v[66:69], v213, s[22:23] offset:528
	global_load_dwordx4 v[70:73], v213, s[22:23] offset:512
	v_readlane_b32 s22, v255, 3
	v_readlane_b32 s23, v255, 4
	v_lshlrev_b32_e32 v247, 12, v246
	v_lshlrev_b32_e32 v246, 13, v246
	v_lshl_add_u32 v247, v212, 1, v247
	v_lshl_add_u32 v246, v212, 2, v246
	s_nop 1
	global_load_dwordx4 v[146:149], v246, s[68:69]
	global_load_dwordx4 v[150:153], v246, s[68:69] offset:16
	global_load_dwordx4 v[154:157], v246, s[68:69] offset:512
	global_load_dwordx4 v[158:161], v246, s[68:69] offset:528
	v_add_u32_e32 v246, 0x20000, v246
	global_load_dwordx4 v[162:165], v246, s[68:69]
	global_load_dwordx4 v[166:169], v246, s[68:69] offset:16
	global_load_dwordx4 v[170:173], v246, s[68:69] offset:512
	global_load_dwordx4 v[174:177], v246, s[68:69] offset:528
	v_add_u32_e32 v246, 0x20000, v246
	global_load_dwordx4 v[178:181], v246, s[68:69]
	global_load_dwordx4 v[182:185], v246, s[68:69] offset:16
	global_load_dwordx4 v[186:189], v246, s[68:69] offset:512
	global_load_dwordx4 v[190:193], v246, s[68:69] offset:528
	v_add_u32_e32 v246, 0x20000, v246
	global_load_dwordx4 v[208:211], v246, s[68:69]
	global_load_dwordx4 v[228:231], v246, s[68:69] offset:16
	global_load_dwordx4 v[232:235], v246, s[68:69] offset:512
	global_load_dwordx4 v[238:241], v246, s[68:69] offset:528
	v_add_u32_e32 v246, 0xa0000, v246
	global_load_dwordx4 v[242:245], v246, s[68:69]
	global_load_dwordx4 v[250:253], v246, s[68:69] offset:16
	s_waitcnt vmcnt(18)
	s_waitcnt vmcnt(16)
	v_pk_fma_f32 v[146:147], v[142:143], v[78:79], v[146:147]
	v_pk_fma_f32 v[148:149], v[144:145], v[80:81], v[148:149]
	v_pk_fma_f32 v[150:151], v[138:139], v[74:75], v[150:151]
	v_pk_fma_f32 v[152:153], v[140:141], v[76:77], v[152:153]
	v_cvt_pk_f16_f32 v146, v146, v147
	v_cvt_pk_f16_f32 v147, v148, v149
	v_cvt_pk_f16_f32 v148, v150, v151
	v_cvt_pk_f16_f32 v149, v152, v153
	global_store_dwordx4 v247, v[146:149], s[22:23]
	global_load_dwordx4 v[142:145], v246, s[68:69] offset:512
	global_load_dwordx4 v[138:141], v246, s[68:69] offset:528
	s_waitcnt vmcnt(17)
	v_pk_fma_f32 v[154:155], v[134:135], v[70:71], v[154:155]
	v_pk_fma_f32 v[156:157], v[136:137], v[72:73], v[156:157]
	v_pk_fma_f32 v[158:159], v[130:131], v[66:67], v[158:159]
	v_pk_fma_f32 v[160:161], v[132:133], v[68:69], v[160:161]
	v_cvt_pk_f16_f32 v154, v154, v155
	v_cvt_pk_f16_f32 v155, v156, v157
	v_cvt_pk_f16_f32 v156, v158, v159
	v_cvt_pk_f16_f32 v157, v160, v161
	global_store_dwordx4 v247, v[154:157], s[22:23] offset:256
	v_add_u32_e32 v246, 0x20000, v246
	global_load_dwordx4 v[134:137], v246, s[68:69]
	global_load_dwordx4 v[130:133], v246, s[68:69] offset:16
	s_waitcnt vmcnt(18)
	v_pk_fma_f32 v[162:163], v[126:127], v[78:79], v[162:163]
	v_pk_fma_f32 v[164:165], v[128:129], v[80:81], v[164:165]
	v_pk_fma_f32 v[166:167], v[122:123], v[74:75], v[166:167]
	v_pk_fma_f32 v[168:169], v[124:125], v[76:77], v[168:169]
	v_cvt_pk_f16_f32 v162, v162, v163
	v_cvt_pk_f16_f32 v163, v164, v165
	v_cvt_pk_f16_f32 v164, v166, v167
	v_cvt_pk_f16_f32 v165, v168, v169
	v_add_u32_e32 v247, 0x10000, v247
	global_store_dwordx4 v247, v[162:165], s[22:23]
	global_load_dwordx4 v[126:129], v246, s[68:69] offset:512
	global_load_dwordx4 v[122:125], v246, s[68:69] offset:528
	s_waitcnt vmcnt(19)
	v_pk_fma_f32 v[170:171], v[118:119], v[70:71], v[170:171]
	v_pk_fma_f32 v[172:173], v[120:121], v[72:73], v[172:173]
	v_pk_fma_f32 v[174:175], v[114:115], v[66:67], v[174:175]
	v_pk_fma_f32 v[176:177], v[116:117], v[68:69], v[176:177]
	v_cvt_pk_f16_f32 v170, v170, v171
	v_cvt_pk_f16_f32 v171, v172, v173
	v_cvt_pk_f16_f32 v172, v174, v175
	v_cvt_pk_f16_f32 v173, v176, v177
	global_store_dwordx4 v247, v[170:173], s[22:23] offset:256
	v_add_u32_e32 v246, 0x20000, v246
	global_load_dwordx4 v[118:121], v246, s[68:69]
	global_load_dwordx4 v[114:117], v246, s[68:69] offset:16
	s_waitcnt vmcnt(20)
	v_pk_fma_f32 v[178:179], v[110:111], v[78:79], v[178:179]
	v_pk_fma_f32 v[180:181], v[112:113], v[80:81], v[180:181]
	v_pk_fma_f32 v[182:183], v[106:107], v[74:75], v[182:183]
	v_pk_fma_f32 v[184:185], v[108:109], v[76:77], v[184:185]
	v_cvt_pk_f16_f32 v178, v178, v179
	v_cvt_pk_f16_f32 v179, v180, v181
	v_cvt_pk_f16_f32 v180, v182, v183
	v_cvt_pk_f16_f32 v181, v184, v185
	v_add_u32_e32 v247, 0x10000, v247
	global_store_dwordx4 v247, v[178:181], s[22:23]
	global_load_dwordx4 v[110:113], v246, s[68:69] offset:512
	global_load_dwordx4 v[106:109], v246, s[68:69] offset:528
	s_waitcnt vmcnt(21)
	v_pk_fma_f32 v[186:187], v[102:103], v[70:71], v[186:187]
	v_pk_fma_f32 v[188:189], v[104:105], v[72:73], v[188:189]
	v_pk_fma_f32 v[190:191], v[98:99], v[66:67], v[190:191]
	v_pk_fma_f32 v[192:193], v[100:101], v[68:69], v[192:193]
	v_cvt_pk_f16_f32 v186, v186, v187
	v_cvt_pk_f16_f32 v187, v188, v189
	v_cvt_pk_f16_f32 v188, v190, v191
	v_cvt_pk_f16_f32 v189, v192, v193
	global_store_dwordx4 v247, v[186:189], s[22:23] offset:256
	v_add_u32_e32 v246, 0x20000, v246
	global_load_dwordx4 v[102:105], v246, s[68:69]
	global_load_dwordx4 v[98:101], v246, s[68:69] offset:16
	s_waitcnt vmcnt(22)
	v_pk_fma_f32 v[208:209], v[94:95], v[78:79], v[208:209]
	v_pk_fma_f32 v[210:211], v[96:97], v[80:81], v[210:211]
	v_pk_fma_f32 v[228:229], v[90:91], v[74:75], v[228:229]
	v_pk_fma_f32 v[230:231], v[92:93], v[76:77], v[230:231]
	v_cvt_pk_f16_f32 v208, v208, v209
	v_cvt_pk_f16_f32 v209, v210, v211
	v_cvt_pk_f16_f32 v210, v228, v229
	v_cvt_pk_f16_f32 v211, v230, v231
	v_add_u32_e32 v247, 0x10000, v247
	global_store_dwordx4 v247, v[208:211], s[22:23]
	global_load_dwordx4 v[94:97], v246, s[68:69] offset:512
	global_load_dwordx4 v[90:93], v246, s[68:69] offset:528
	s_waitcnt vmcnt(23)
	v_pk_fma_f32 v[232:233], v[86:87], v[70:71], v[232:233]
	v_pk_fma_f32 v[234:235], v[88:89], v[72:73], v[234:235]
	v_pk_fma_f32 v[238:239], v[82:83], v[66:67], v[238:239]
	v_pk_fma_f32 v[240:241], v[84:85], v[68:69], v[240:241]
	v_cvt_pk_f16_f32 v232, v232, v233
	v_cvt_pk_f16_f32 v233, v234, v235
	v_cvt_pk_f16_f32 v234, v238, v239
	v_cvt_pk_f16_f32 v235, v240, v241
	global_store_dwordx4 v247, v[232:235], s[22:23] offset:256
	s_waitcnt vmcnt(22)
	v_pk_fma_f32 v[242:243], v[62:63], v[78:79], v[242:243]
	v_pk_fma_f32 v[244:245], v[64:65], v[80:81], v[244:245]
	v_pk_fma_f32 v[250:251], v[58:59], v[74:75], v[250:251]
	v_pk_fma_f32 v[252:253], v[60:61], v[76:77], v[252:253]
	v_cvt_pk_f16_f32 v242, v242, v243
	v_cvt_pk_f16_f32 v243, v244, v245
	v_cvt_pk_f16_f32 v244, v250, v251
	v_cvt_pk_f16_f32 v245, v252, v253
	v_add_u32_e32 v247, 0x50000, v247
	global_store_dwordx4 v247, v[242:245], s[22:23]
	s_waitcnt vmcnt(20)
	v_pk_fma_f32 v[142:143], v[54:55], v[70:71], v[142:143]
	v_pk_fma_f32 v[144:145], v[56:57], v[72:73], v[144:145]
	v_pk_fma_f32 v[138:139], v[50:51], v[66:67], v[138:139]
	v_pk_fma_f32 v[140:141], v[52:53], v[68:69], v[140:141]
	v_cvt_pk_f16_f32 v142, v142, v143
	v_cvt_pk_f16_f32 v143, v144, v145
	v_cvt_pk_f16_f32 v144, v138, v139
	v_cvt_pk_f16_f32 v145, v140, v141
	global_store_dwordx4 v247, v[142:145], s[22:23] offset:256
	s_waitcnt vmcnt(18)
	v_pk_fma_f32 v[134:135], v[46:47], v[78:79], v[134:135]
	v_pk_fma_f32 v[136:137], v[48:49], v[80:81], v[136:137]
	v_pk_fma_f32 v[130:131], v[42:43], v[74:75], v[130:131]
	v_pk_fma_f32 v[132:133], v[44:45], v[76:77], v[132:133]
	v_cvt_pk_f16_f32 v134, v134, v135
	v_cvt_pk_f16_f32 v135, v136, v137
	v_cvt_pk_f16_f32 v136, v130, v131
	v_cvt_pk_f16_f32 v137, v132, v133
	v_add_u32_e32 v247, 0x10000, v247
	global_store_dwordx4 v247, v[134:137], s[22:23]
	s_waitcnt vmcnt(16)
	v_pk_fma_f32 v[126:127], v[38:39], v[70:71], v[126:127]
	v_pk_fma_f32 v[128:129], v[40:41], v[72:73], v[128:129]
	v_pk_fma_f32 v[122:123], v[34:35], v[66:67], v[122:123]
	v_pk_fma_f32 v[124:125], v[36:37], v[68:69], v[124:125]
	v_cvt_pk_f16_f32 v126, v126, v127
	v_cvt_pk_f16_f32 v127, v128, v129
	v_cvt_pk_f16_f32 v128, v122, v123
	v_cvt_pk_f16_f32 v129, v124, v125
	global_store_dwordx4 v247, v[126:129], s[22:23] offset:256
	s_waitcnt vmcnt(14)
	v_pk_fma_f32 v[118:119], v[30:31], v[78:79], v[118:119]
	v_pk_fma_f32 v[120:121], v[32:33], v[80:81], v[120:121]
	v_pk_fma_f32 v[114:115], v[26:27], v[74:75], v[114:115]
	v_pk_fma_f32 v[116:117], v[28:29], v[76:77], v[116:117]
	v_cvt_pk_f16_f32 v118, v118, v119
	v_cvt_pk_f16_f32 v119, v120, v121
	v_cvt_pk_f16_f32 v120, v114, v115
	v_cvt_pk_f16_f32 v121, v116, v117
	v_add_u32_e32 v247, 0x10000, v247
	global_store_dwordx4 v247, v[118:121], s[22:23]
	s_waitcnt vmcnt(12)
	v_pk_fma_f32 v[110:111], v[22:23], v[70:71], v[110:111]
	v_pk_fma_f32 v[112:113], v[24:25], v[72:73], v[112:113]
	v_pk_fma_f32 v[106:107], v[18:19], v[66:67], v[106:107]
	v_pk_fma_f32 v[108:109], v[20:21], v[68:69], v[108:109]
	v_cvt_pk_f16_f32 v110, v110, v111
	v_cvt_pk_f16_f32 v111, v112, v113
	v_cvt_pk_f16_f32 v112, v106, v107
	v_cvt_pk_f16_f32 v113, v108, v109
	global_store_dwordx4 v247, v[110:113], s[22:23] offset:256
	s_waitcnt vmcnt(10)
	v_pk_fma_f32 v[102:103], v[14:15], v[78:79], v[102:103]
	v_pk_fma_f32 v[104:105], v[16:17], v[80:81], v[104:105]
	v_pk_fma_f32 v[98:99], v[10:11], v[74:75], v[98:99]
	v_pk_fma_f32 v[100:101], v[12:13], v[76:77], v[100:101]
	v_cvt_pk_f16_f32 v102, v102, v103
	v_cvt_pk_f16_f32 v103, v104, v105
	v_cvt_pk_f16_f32 v104, v98, v99
	v_cvt_pk_f16_f32 v105, v100, v101
	v_add_u32_e32 v247, 0x10000, v247
	global_store_dwordx4 v247, v[102:105], s[22:23]
	s_waitcnt vmcnt(8)
	v_pk_fma_f32 v[94:95], v[6:7], v[70:71], v[94:95]
	v_pk_fma_f32 v[96:97], v[8:9], v[72:73], v[96:97]
	v_pk_fma_f32 v[90:91], v[2:3], v[66:67], v[90:91]
	v_pk_fma_f32 v[92:93], v[4:5], v[68:69], v[92:93]
	v_cvt_pk_f16_f32 v94, v94, v95
	v_cvt_pk_f16_f32 v95, v96, v97
	v_cvt_pk_f16_f32 v96, v90, v91
	v_cvt_pk_f16_f32 v97, v92, v93
	global_store_dwordx4 v247, v[94:97], s[22:23] offset:256
	s_and_b64 vcc, exec, s[4:5]
	s_mov_b64 s[20:21], -1
	s_cbranch_vccnz .LBB0_748
	s_andn2_b64 vcc, exec, s[2:3]
	s_cbranch_vccnz .LBB0_747
	s_barrier
	s_branch .LBB0_747

.LBB0_1062:
	v_readlane_b32 s70, v254, 10
	v_readlane_b32 s71, v254, 11
	v_readlane_b32 s72, v254, 12
	v_readlane_b32 s73, v254, 13
	v_readlane_b32 s74, v254, 14
	v_readlane_b32 s75, v254, 15
	v_readlane_b32 s76, v254, 16
	v_readlane_b32 s77, v254, 17
	v_readlane_b32 s78, v254, 18
	v_readlane_b32 s79, v254, 19
	v_readlane_b32 s80, v254, 20
	v_readlane_b32 s81, v254, 21
	v_readlane_b32 s82, v254, 22
	v_readlane_b32 s83, v254, 23
	s_ashr_i32 s9, s18, 3
	s_mul_hi_i32 s11, s9, 0xc000
	s_mul_i32 s9, s9, 0xc000
	v_lshl_or_b32 v212, s20, 8, v216
	s_add_u32 s22, s43, s9
	s_addc_u32 s23, s44, s11
	v_lshlrev_b32_e32 v213, 2, v212
	v_lshl_add_u32 v246, s18, 8, v1
	v_readlane_b32 s68, v254, 8
	v_readlane_b32 s69, v254, 9
	global_load_dwordx4 v[74:77], v213, s[22:23] offset:16
	global_load_dwordx4 v[78:81], v213, s[22:23]
	global_load_dwordx4 v[66:69], v213, s[22:23] offset:528
	global_load_dwordx4 v[70:73], v213, s[22:23] offset:512
	v_readlane_b32 s22, v255, 3
	v_readlane_b32 s23, v255, 4
	v_lshlrev_b32_e32 v247, 12, v246
	v_lshlrev_b32_e32 v246, 13, v246
	v_lshl_add_u32 v247, v212, 1, v247
	v_lshl_add_u32 v246, v212, 2, v246
	s_nop 1
	global_load_dwordx4 v[146:149], v246, s[68:69]
	global_load_dwordx4 v[150:153], v246, s[68:69] offset:16
	global_load_dwordx4 v[154:157], v246, s[68:69] offset:512
	global_load_dwordx4 v[158:161], v246, s[68:69] offset:528
	v_add_u32_e32 v246, 0x20000, v246
	global_load_dwordx4 v[162:165], v246, s[68:69]
	global_load_dwordx4 v[166:169], v246, s[68:69] offset:16
	global_load_dwordx4 v[170:173], v246, s[68:69] offset:512
	global_load_dwordx4 v[174:177], v246, s[68:69] offset:528
	v_add_u32_e32 v246, 0x20000, v246
	global_load_dwordx4 v[178:181], v246, s[68:69]
	global_load_dwordx4 v[182:185], v246, s[68:69] offset:16
	global_load_dwordx4 v[186:189], v246, s[68:69] offset:512
	global_load_dwordx4 v[190:193], v246, s[68:69] offset:528
	v_add_u32_e32 v246, 0x20000, v246
	global_load_dwordx4 v[208:211], v246, s[68:69]
	global_load_dwordx4 v[228:231], v246, s[68:69] offset:16
	global_load_dwordx4 v[232:235], v246, s[68:69] offset:512
	global_load_dwordx4 v[238:241], v246, s[68:69] offset:528
	v_add_u32_e32 v246, 0xa0000, v246
	global_load_dwordx4 v[242:245], v246, s[68:69]
	global_load_dwordx4 v[250:253], v246, s[68:69] offset:16
	s_waitcnt vmcnt(18)
	s_waitcnt vmcnt(16)
	v_pk_fma_f32 v[146:147], v[142:143], v[78:79], v[146:147]
	v_pk_fma_f32 v[148:149], v[144:145], v[80:81], v[148:149]
	v_pk_fma_f32 v[150:151], v[138:139], v[74:75], v[150:151]
	v_pk_fma_f32 v[152:153], v[140:141], v[76:77], v[152:153]
	v_cvt_pk_f16_f32 v146, v146, v147
	v_cvt_pk_f16_f32 v147, v148, v149
	v_cvt_pk_f16_f32 v148, v150, v151
	v_cvt_pk_f16_f32 v149, v152, v153
	global_store_dwordx4 v247, v[146:149], s[22:23]
	global_load_dwordx4 v[142:145], v246, s[68:69] offset:512
	global_load_dwordx4 v[138:141], v246, s[68:69] offset:528
	s_waitcnt vmcnt(17)
	v_pk_fma_f32 v[154:155], v[134:135], v[70:71], v[154:155]
	v_pk_fma_f32 v[156:157], v[136:137], v[72:73], v[156:157]
	v_pk_fma_f32 v[158:159], v[130:131], v[66:67], v[158:159]
	v_pk_fma_f32 v[160:161], v[132:133], v[68:69], v[160:161]
	v_cvt_pk_f16_f32 v154, v154, v155
	v_cvt_pk_f16_f32 v155, v156, v157
	v_cvt_pk_f16_f32 v156, v158, v159
	v_cvt_pk_f16_f32 v157, v160, v161
	global_store_dwordx4 v247, v[154:157], s[22:23] offset:256
	v_add_u32_e32 v246, 0x20000, v246
	global_load_dwordx4 v[134:137], v246, s[68:69]
	global_load_dwordx4 v[130:133], v246, s[68:69] offset:16
	s_waitcnt vmcnt(18)
	v_pk_fma_f32 v[162:163], v[126:127], v[78:79], v[162:163]
	v_pk_fma_f32 v[164:165], v[128:129], v[80:81], v[164:165]
	v_pk_fma_f32 v[166:167], v[122:123], v[74:75], v[166:167]
	v_pk_fma_f32 v[168:169], v[124:125], v[76:77], v[168:169]
	v_cvt_pk_f16_f32 v162, v162, v163
	v_cvt_pk_f16_f32 v163, v164, v165
	v_cvt_pk_f16_f32 v164, v166, v167
	v_cvt_pk_f16_f32 v165, v168, v169
	v_add_u32_e32 v247, 0x10000, v247
	global_store_dwordx4 v247, v[162:165], s[22:23]
	global_load_dwordx4 v[126:129], v246, s[68:69] offset:512
	global_load_dwordx4 v[122:125], v246, s[68:69] offset:528
	s_waitcnt vmcnt(19)
	v_pk_fma_f32 v[170:171], v[118:119], v[70:71], v[170:171]
	v_pk_fma_f32 v[172:173], v[120:121], v[72:73], v[172:173]
	v_pk_fma_f32 v[174:175], v[114:115], v[66:67], v[174:175]
	v_pk_fma_f32 v[176:177], v[116:117], v[68:69], v[176:177]
	v_cvt_pk_f16_f32 v170, v170, v171
	v_cvt_pk_f16_f32 v171, v172, v173
	v_cvt_pk_f16_f32 v172, v174, v175
	v_cvt_pk_f16_f32 v173, v176, v177
	global_store_dwordx4 v247, v[170:173], s[22:23] offset:256
	v_add_u32_e32 v246, 0x20000, v246
	global_load_dwordx4 v[118:121], v246, s[68:69]
	global_load_dwordx4 v[114:117], v246, s[68:69] offset:16
	s_waitcnt vmcnt(20)
	v_pk_fma_f32 v[178:179], v[110:111], v[78:79], v[178:179]
	v_pk_fma_f32 v[180:181], v[112:113], v[80:81], v[180:181]
	v_pk_fma_f32 v[182:183], v[106:107], v[74:75], v[182:183]
	v_pk_fma_f32 v[184:185], v[108:109], v[76:77], v[184:185]
	v_cvt_pk_f16_f32 v178, v178, v179
	v_cvt_pk_f16_f32 v179, v180, v181
	v_cvt_pk_f16_f32 v180, v182, v183
	v_cvt_pk_f16_f32 v181, v184, v185
	v_add_u32_e32 v247, 0x10000, v247
	global_store_dwordx4 v247, v[178:181], s[22:23]
	global_load_dwordx4 v[110:113], v246, s[68:69] offset:512
	global_load_dwordx4 v[106:109], v246, s[68:69] offset:528
	s_waitcnt vmcnt(21)
	v_pk_fma_f32 v[186:187], v[102:103], v[70:71], v[186:187]
	v_pk_fma_f32 v[188:189], v[104:105], v[72:73], v[188:189]
	v_pk_fma_f32 v[190:191], v[98:99], v[66:67], v[190:191]
	v_pk_fma_f32 v[192:193], v[100:101], v[68:69], v[192:193]
	v_cvt_pk_f16_f32 v186, v186, v187
	v_cvt_pk_f16_f32 v187, v188, v189
	v_cvt_pk_f16_f32 v188, v190, v191
	v_cvt_pk_f16_f32 v189, v192, v193
	global_store_dwordx4 v247, v[186:189], s[22:23] offset:256
	v_add_u32_e32 v246, 0x20000, v246
	global_load_dwordx4 v[102:105], v246, s[68:69]
	global_load_dwordx4 v[98:101], v246, s[68:69] offset:16
	s_waitcnt vmcnt(22)
	v_pk_fma_f32 v[208:209], v[94:95], v[78:79], v[208:209]
	v_pk_fma_f32 v[210:211], v[96:97], v[80:81], v[210:211]
	v_pk_fma_f32 v[228:229], v[90:91], v[74:75], v[228:229]
	v_pk_fma_f32 v[230:231], v[92:93], v[76:77], v[230:231]
	v_cvt_pk_f16_f32 v208, v208, v209
	v_cvt_pk_f16_f32 v209, v210, v211
	v_cvt_pk_f16_f32 v210, v228, v229
	v_cvt_pk_f16_f32 v211, v230, v231
	v_add_u32_e32 v247, 0x10000, v247
	global_store_dwordx4 v247, v[208:211], s[22:23]
	global_load_dwordx4 v[94:97], v246, s[68:69] offset:512
	global_load_dwordx4 v[90:93], v246, s[68:69] offset:528
	s_waitcnt vmcnt(23)
	v_pk_fma_f32 v[232:233], v[86:87], v[70:71], v[232:233]
	v_pk_fma_f32 v[234:235], v[88:89], v[72:73], v[234:235]
	v_pk_fma_f32 v[238:239], v[82:83], v[66:67], v[238:239]
	v_pk_fma_f32 v[240:241], v[84:85], v[68:69], v[240:241]
	v_cvt_pk_f16_f32 v232, v232, v233
	v_cvt_pk_f16_f32 v233, v234, v235
	v_cvt_pk_f16_f32 v234, v238, v239
	v_cvt_pk_f16_f32 v235, v240, v241
	global_store_dwordx4 v247, v[232:235], s[22:23] offset:256
	s_waitcnt vmcnt(22)
	v_pk_fma_f32 v[242:243], v[62:63], v[78:79], v[242:243]
	v_pk_fma_f32 v[244:245], v[64:65], v[80:81], v[244:245]
	v_pk_fma_f32 v[250:251], v[58:59], v[74:75], v[250:251]
	v_pk_fma_f32 v[252:253], v[60:61], v[76:77], v[252:253]
	v_cvt_pk_f16_f32 v242, v242, v243
	v_cvt_pk_f16_f32 v243, v244, v245
	v_cvt_pk_f16_f32 v244, v250, v251
	v_cvt_pk_f16_f32 v245, v252, v253
	v_add_u32_e32 v247, 0x50000, v247
	global_store_dwordx4 v247, v[242:245], s[22:23]
	s_waitcnt vmcnt(20)
	v_pk_fma_f32 v[142:143], v[54:55], v[70:71], v[142:143]
	v_pk_fma_f32 v[144:145], v[56:57], v[72:73], v[144:145]
	v_pk_fma_f32 v[138:139], v[50:51], v[66:67], v[138:139]
	v_pk_fma_f32 v[140:141], v[52:53], v[68:69], v[140:141]
	v_cvt_pk_f16_f32 v142, v142, v143
	v_cvt_pk_f16_f32 v143, v144, v145
	v_cvt_pk_f16_f32 v144, v138, v139
	v_cvt_pk_f16_f32 v145, v140, v141
	global_store_dwordx4 v247, v[142:145], s[22:23] offset:256
	s_waitcnt vmcnt(18)
	v_pk_fma_f32 v[134:135], v[46:47], v[78:79], v[134:135]
	v_pk_fma_f32 v[136:137], v[48:49], v[80:81], v[136:137]
	v_pk_fma_f32 v[130:131], v[42:43], v[74:75], v[130:131]
	v_pk_fma_f32 v[132:133], v[44:45], v[76:77], v[132:133]
	v_cvt_pk_f16_f32 v134, v134, v135
	v_cvt_pk_f16_f32 v135, v136, v137
	v_cvt_pk_f16_f32 v136, v130, v131
	v_cvt_pk_f16_f32 v137, v132, v133
	v_add_u32_e32 v247, 0x10000, v247
	global_store_dwordx4 v247, v[134:137], s[22:23]
	s_waitcnt vmcnt(16)
	v_pk_fma_f32 v[126:127], v[38:39], v[70:71], v[126:127]
	v_pk_fma_f32 v[128:129], v[40:41], v[72:73], v[128:129]
	v_pk_fma_f32 v[122:123], v[34:35], v[66:67], v[122:123]
	v_pk_fma_f32 v[124:125], v[36:37], v[68:69], v[124:125]
	v_cvt_pk_f16_f32 v126, v126, v127
	v_cvt_pk_f16_f32 v127, v128, v129
	v_cvt_pk_f16_f32 v128, v122, v123
	v_cvt_pk_f16_f32 v129, v124, v125
	global_store_dwordx4 v247, v[126:129], s[22:23] offset:256
	s_waitcnt vmcnt(14)
	v_pk_fma_f32 v[118:119], v[30:31], v[78:79], v[118:119]
	v_pk_fma_f32 v[120:121], v[32:33], v[80:81], v[120:121]
	v_pk_fma_f32 v[114:115], v[26:27], v[74:75], v[114:115]
	v_pk_fma_f32 v[116:117], v[28:29], v[76:77], v[116:117]
	v_cvt_pk_f16_f32 v118, v118, v119
	v_cvt_pk_f16_f32 v119, v120, v121
	v_cvt_pk_f16_f32 v120, v114, v115
	v_cvt_pk_f16_f32 v121, v116, v117
	v_add_u32_e32 v247, 0x10000, v247
	global_store_dwordx4 v247, v[118:121], s[22:23]
	s_waitcnt vmcnt(12)
	v_pk_fma_f32 v[110:111], v[22:23], v[70:71], v[110:111]
	v_pk_fma_f32 v[112:113], v[24:25], v[72:73], v[112:113]
	v_pk_fma_f32 v[106:107], v[18:19], v[66:67], v[106:107]
	v_pk_fma_f32 v[108:109], v[20:21], v[68:69], v[108:109]
	v_cvt_pk_f16_f32 v110, v110, v111
	v_cvt_pk_f16_f32 v111, v112, v113
	v_cvt_pk_f16_f32 v112, v106, v107
	v_cvt_pk_f16_f32 v113, v108, v109
	global_store_dwordx4 v247, v[110:113], s[22:23] offset:256
	s_waitcnt vmcnt(10)
	v_pk_fma_f32 v[102:103], v[14:15], v[78:79], v[102:103]
	v_pk_fma_f32 v[104:105], v[16:17], v[80:81], v[104:105]
	v_pk_fma_f32 v[98:99], v[10:11], v[74:75], v[98:99]
	v_pk_fma_f32 v[100:101], v[12:13], v[76:77], v[100:101]
	v_cvt_pk_f16_f32 v102, v102, v103
	v_cvt_pk_f16_f32 v103, v104, v105
	v_cvt_pk_f16_f32 v104, v98, v99
	v_cvt_pk_f16_f32 v105, v100, v101
	v_add_u32_e32 v247, 0x10000, v247
	global_store_dwordx4 v247, v[102:105], s[22:23]
	s_waitcnt vmcnt(8)
	v_pk_fma_f32 v[94:95], v[6:7], v[70:71], v[94:95]
	v_pk_fma_f32 v[96:97], v[8:9], v[72:73], v[96:97]
	v_pk_fma_f32 v[90:91], v[2:3], v[66:67], v[90:91]
	v_pk_fma_f32 v[92:93], v[4:5], v[68:69], v[92:93]
	v_cvt_pk_f16_f32 v94, v94, v95
	v_cvt_pk_f16_f32 v95, v96, v97
	v_cvt_pk_f16_f32 v96, v90, v91
	v_cvt_pk_f16_f32 v97, v92, v93
	global_store_dwordx4 v247, v[94:97], s[22:23] offset:256
	s_andn2_b64 vcc, exec, s[14:15]
	s_mov_b64 s[18:19], -1
	s_cbranch_vccnz .LBB0_1041
	s_andn2_b64 vcc, exec, s[0:1]
	s_cbranch_vccnz .LBB0_1040
	s_barrier
	s_branch .LBB0_1040
